# LN1/router: s_setprio raise for the wave running the serial top-4 (the group's straggler), lowered again after it
# speedup vs baseline: 1.0011x; 1.0011x over previous
; #define LAS __attribute__((address_space(3)))
; template <bool SKIP_MIX>
; __device__ __forceinline__ void p8_ln_router(Frame& F0, const In& I) {
;     ...
;         f32x4 c0 = (f32x4){0.f, 0.f, 0.f, 0.f}, c1 = c0;
;         const LAS float* ap = hs + col * P8_PITCH + 256 * w + 4 * kq;
;         const float* bp = I.w_router + (size_t)(256 * w + 4 * kq) * NE + col;
; #pragma unroll 4
;         for (int kk = 0; kk < 16; ++kk) {
;             const f32x4 a = *(const LAS f32x4*)(ap + 16 * kk);
; #pragma unroll
;             for (int e = 0; e < 4; ++e) {
;                 const float b0 = bp[(size_t)(16 * kk + e) * NE], b1 = bp[(size_t)(16 * kk + e) * NE + 16];
;                 c0 = __builtin_amdgcn_mfma_f32_16x16x4f32(a[e], b0, c0, 0, 0, 0);
;                 c1 = __builtin_amdgcn_mfma_f32_16x16x4f32(a[e], b1, c1, 0, 0, 0);
;             }
;         }
.LBB0_1515:
	s_waitcnt vmcnt(19)
	s_mov_b64 s[0:1], 0x1000
	v_mov_b32_e32 v108, v88
	v_mov_b32_e32 v109, v89
	global_load_dword v117, v[108:109], off offset:0
	global_load_dword v118, v[108:109], off offset:64
	global_load_dword v119, v[108:109], off offset:128
	global_load_dword v120, v[108:109], off offset:192
	global_load_dword v121, v[108:109], off offset:256
	global_load_dword v122, v[108:109], off offset:320
	global_load_dword v123, v[108:109], off offset:384
	global_load_dword v124, v[108:109], off offset:448
	global_load_dword v125, v[108:109], off offset:2048
	global_load_dword v126, v[108:109], off offset:2112
	global_load_dword v127, v[108:109], off offset:2176
	global_load_dword v128, v[108:109], off offset:2240
	global_load_dword v129, v[108:109], off offset:2304
	global_load_dword v130, v[108:109], off offset:2368
	global_load_dword v131, v[108:109], off offset:2432
	global_load_dword v132, v[108:109], off offset:2496
	v_lshl_add_u64 v[108:109], v[108:109], 0, s[0:1]
	global_load_dword v133, v[108:109], off offset:0
	global_load_dword v134, v[108:109], off offset:64
	global_load_dword v135, v[108:109], off offset:128
	global_load_dword v136, v[108:109], off offset:192
	global_load_dword v137, v[108:109], off offset:256
	global_load_dword v138, v[108:109], off offset:320
	global_load_dword v139, v[108:109], off offset:384
	global_load_dword v140, v[108:109], off offset:448
	global_load_dword v141, v[108:109], off offset:2048
	global_load_dword v142, v[108:109], off offset:2112
	global_load_dword v143, v[108:109], off offset:2176
	global_load_dword v144, v[108:109], off offset:2240
	global_load_dword v145, v[108:109], off offset:2304
	global_load_dword v146, v[108:109], off offset:2368
	global_load_dword v147, v[108:109], off offset:2432
	global_load_dword v148, v[108:109], off offset:2496
	v_lshl_add_u64 v[108:109], v[108:109], 0, s[0:1]
	global_load_dword v149, v[108:109], off offset:0
	global_load_dword v150, v[108:109], off offset:64
	global_load_dword v151, v[108:109], off offset:128
	global_load_dword v160, v[108:109], off offset:192
	global_load_dword v161, v[108:109], off offset:256
	global_load_dword v162, v[108:109], off offset:320
	global_load_dword v163, v[108:109], off offset:384
	global_load_dword v164, v[108:109], off offset:448
	global_load_dword v165, v[108:109], off offset:2048
	global_load_dword v166, v[108:109], off offset:2112
	global_load_dword v167, v[108:109], off offset:2176
	global_load_dword v168, v[108:109], off offset:2240
	ds_read_b128 v[92:95], v90
	ds_read_b128 v[96:99], v90 offset:64
	ds_read_b128 v[100:103], v90 offset:128
	ds_read_b128 v[104:107], v90 offset:192
	s_waitcnt lgkmcnt(3)
	global_load_dword v169, v[108:109], off offset:2304
	s_waitcnt vmcnt(43)
	v_mfma_f32_16x16x4_f32 v[66:69], v92, v117, v[66:69]
	v_mfma_f32_16x16x4_f32 v[70:73], v92, v118, v[70:73]
	global_load_dword v170, v[108:109], off offset:2368
	s_waitcnt vmcnt(42)
	v_mfma_f32_16x16x4_f32 v[66:69], v93, v119, v[66:69]
	v_mfma_f32_16x16x4_f32 v[70:73], v93, v120, v[70:73]
	global_load_dword v171, v[108:109], off offset:2432
	s_waitcnt vmcnt(41)
	v_mfma_f32_16x16x4_f32 v[66:69], v94, v121, v[66:69]
	v_mfma_f32_16x16x4_f32 v[70:73], v94, v122, v[70:73]
	global_load_dword v172, v[108:109], off offset:2496
	s_waitcnt vmcnt(40)
	v_mfma_f32_16x16x4_f32 v[66:69], v95, v123, v[66:69]
	v_mfma_f32_16x16x4_f32 v[70:73], v95, v124, v[70:73]
	s_waitcnt lgkmcnt(2)
	v_lshl_add_u64 v[108:109], v[108:109], 0, s[0:1]
	global_load_dword v173, v[108:109], off offset:0
	s_waitcnt vmcnt(39)
	v_mfma_f32_16x16x4_f32 v[66:69], v96, v125, v[66:69]
	v_mfma_f32_16x16x4_f32 v[70:73], v96, v126, v[70:73]
	global_load_dword v174, v[108:109], off offset:64
	s_waitcnt vmcnt(38)
	v_mfma_f32_16x16x4_f32 v[66:69], v97, v127, v[66:69]
	v_mfma_f32_16x16x4_f32 v[70:73], v97, v128, v[70:73]
	global_load_dword v175, v[108:109], off offset:128
	s_waitcnt vmcnt(37)
	v_mfma_f32_16x16x4_f32 v[66:69], v98, v129, v[66:69]
	v_mfma_f32_16x16x4_f32 v[70:73], v98, v130, v[70:73]
	global_load_dword v176, v[108:109], off offset:192
	s_waitcnt vmcnt(36)
	v_mfma_f32_16x16x4_f32 v[66:69], v99, v131, v[66:69]
	v_mfma_f32_16x16x4_f32 v[70:73], v99, v132, v[70:73]
	s_waitcnt lgkmcnt(1)
	global_load_dword v177, v[108:109], off offset:256
	s_waitcnt vmcnt(35)
	v_mfma_f32_16x16x4_f32 v[66:69], v100, v133, v[66:69]
	v_mfma_f32_16x16x4_f32 v[70:73], v100, v134, v[70:73]
	global_load_dword v178, v[108:109], off offset:320
	s_waitcnt vmcnt(34)
	v_mfma_f32_16x16x4_f32 v[66:69], v101, v135, v[66:69]
	v_mfma_f32_16x16x4_f32 v[70:73], v101, v136, v[70:73]
	global_load_dword v179, v[108:109], off offset:384
	s_waitcnt vmcnt(33)
	v_mfma_f32_16x16x4_f32 v[66:69], v102, v137, v[66:69]
	v_mfma_f32_16x16x4_f32 v[70:73], v102, v138, v[70:73]
	global_load_dword v180, v[108:109], off offset:448
	s_waitcnt vmcnt(32)
	v_mfma_f32_16x16x4_f32 v[66:69], v103, v139, v[66:69]
	v_mfma_f32_16x16x4_f32 v[70:73], v103, v140, v[70:73]
	s_waitcnt lgkmcnt(0)
	global_load_dword v181, v[108:109], off offset:2048
	s_waitcnt vmcnt(31)
	v_mfma_f32_16x16x4_f32 v[66:69], v104, v141, v[66:69]
	v_mfma_f32_16x16x4_f32 v[70:73], v104, v142, v[70:73]
	global_load_dword v182, v[108:109], off offset:2112
	s_waitcnt vmcnt(30)
	v_mfma_f32_16x16x4_f32 v[66:69], v105, v143, v[66:69]
	v_mfma_f32_16x16x4_f32 v[70:73], v105, v144, v[70:73]
	global_load_dword v183, v[108:109], off offset:2176
	s_waitcnt vmcnt(29)
	v_mfma_f32_16x16x4_f32 v[66:69], v106, v145, v[66:69]
	v_mfma_f32_16x16x4_f32 v[70:73], v106, v146, v[70:73]
	global_load_dword v184, v[108:109], off offset:2240
	s_waitcnt vmcnt(28)
; #define LAS __attribute__((address_space(3)))
; template <bool SKIP_MIX>
; __device__ __forceinline__ void p8_ln_router(Frame& F0, const In& I) {
;     ...
;         for (int kk = 0; kk < 16; ++kk) {
;             const f32x4 a = *(const LAS f32x4*)(ap + 16 * kk);
; #pragma unroll
;             for (int e = 0; e < 4; ++e) {
;                 const float b0 = bp[(size_t)(16 * kk + e) * NE], b1 = bp[(size_t)(16 * kk + e) * NE + 16];
;                 c0 = __builtin_amdgcn_mfma_f32_16x16x4f32(a[e], b0, c0, 0, 0, 0);
;                 c1 = __builtin_amdgcn_mfma_f32_16x16x4f32(a[e], b1, c1, 0, 0, 0);
;             }
;         }
	v_mfma_f32_16x16x4_f32 v[66:69], v107, v147, v[66:69]
	v_mfma_f32_16x16x4_f32 v[70:73], v107, v148, v[70:73]
	ds_read_b128 v[92:95], v90 offset:256
	ds_read_b128 v[96:99], v90 offset:320
	ds_read_b128 v[100:103], v90 offset:384
	ds_read_b128 v[104:107], v90 offset:448
	s_waitcnt lgkmcnt(3)
	global_load_dword v185, v[108:109], off offset:2304
	s_waitcnt vmcnt(27)
	v_mfma_f32_16x16x4_f32 v[66:69], v92, v149, v[66:69]
	v_mfma_f32_16x16x4_f32 v[70:73], v92, v150, v[70:73]
	global_load_dword v186, v[108:109], off offset:2368
	s_waitcnt vmcnt(26)
	v_mfma_f32_16x16x4_f32 v[66:69], v93, v151, v[66:69]
	v_mfma_f32_16x16x4_f32 v[70:73], v93, v160, v[70:73]
	global_load_dword v187, v[108:109], off offset:2432
	s_waitcnt vmcnt(25)
	v_mfma_f32_16x16x4_f32 v[66:69], v94, v161, v[66:69]
	v_mfma_f32_16x16x4_f32 v[70:73], v94, v162, v[70:73]
	global_load_dword v188, v[108:109], off offset:2496
	s_waitcnt vmcnt(24)
	v_mfma_f32_16x16x4_f32 v[66:69], v95, v163, v[66:69]
	v_mfma_f32_16x16x4_f32 v[70:73], v95, v164, v[70:73]
	s_waitcnt lgkmcnt(2)
	v_lshl_add_u64 v[108:109], v[108:109], 0, s[0:1]
	global_load_dword v189, v[108:109], off offset:0
	s_waitcnt vmcnt(23)
	v_mfma_f32_16x16x4_f32 v[66:69], v96, v165, v[66:69]
	v_mfma_f32_16x16x4_f32 v[70:73], v96, v166, v[70:73]
	global_load_dword v190, v[108:109], off offset:64
	s_waitcnt vmcnt(22)
	v_mfma_f32_16x16x4_f32 v[66:69], v97, v167, v[66:69]
	v_mfma_f32_16x16x4_f32 v[70:73], v97, v168, v[70:73]
	global_load_dword v191, v[108:109], off offset:128
	s_waitcnt vmcnt(21)
	v_mfma_f32_16x16x4_f32 v[66:69], v98, v169, v[66:69]
	v_mfma_f32_16x16x4_f32 v[70:73], v98, v170, v[70:73]
	global_load_dword v192, v[108:109], off offset:192
	s_waitcnt vmcnt(20)
	v_mfma_f32_16x16x4_f32 v[66:69], v99, v171, v[66:69]
	v_mfma_f32_16x16x4_f32 v[70:73], v99, v172, v[70:73]
	s_waitcnt lgkmcnt(1)
	global_load_dword v193, v[108:109], off offset:256
	s_waitcnt vmcnt(19)
	v_mfma_f32_16x16x4_f32 v[66:69], v100, v173, v[66:69]
	v_mfma_f32_16x16x4_f32 v[70:73], v100, v174, v[70:73]
	global_load_dword v194, v[108:109], off offset:320
	s_waitcnt vmcnt(18)
	v_mfma_f32_16x16x4_f32 v[66:69], v101, v175, v[66:69]
	v_mfma_f32_16x16x4_f32 v[70:73], v101, v176, v[70:73]
	global_load_dword v195, v[108:109], off offset:384
	s_waitcnt vmcnt(17)
	v_mfma_f32_16x16x4_f32 v[66:69], v102, v177, v[66:69]
	v_mfma_f32_16x16x4_f32 v[70:73], v102, v178, v[70:73]
	global_load_dword v196, v[108:109], off offset:448
	s_waitcnt vmcnt(16)
	v_mfma_f32_16x16x4_f32 v[66:69], v103, v179, v[66:69]
	v_mfma_f32_16x16x4_f32 v[70:73], v103, v180, v[70:73]
	s_waitcnt lgkmcnt(0)
	global_load_dword v197, v[108:109], off offset:2048
	s_waitcnt vmcnt(15)
	v_mfma_f32_16x16x4_f32 v[66:69], v104, v181, v[66:69]
	v_mfma_f32_16x16x4_f32 v[70:73], v104, v182, v[70:73]
	global_load_dword v198, v[108:109], off offset:2112
	s_waitcnt vmcnt(14)
	v_mfma_f32_16x16x4_f32 v[66:69], v105, v183, v[66:69]
	v_mfma_f32_16x16x4_f32 v[70:73], v105, v184, v[70:73]
	global_load_dword v199, v[108:109], off offset:2176
	s_waitcnt vmcnt(13)
	v_mfma_f32_16x16x4_f32 v[66:69], v106, v185, v[66:69]
	v_mfma_f32_16x16x4_f32 v[70:73], v106, v186, v[70:73]
	s_waitcnt vmcnt(11)
	v_mfma_f32_16x16x4_f32 v[66:69], v107, v187, v[66:69]
	v_mfma_f32_16x16x4_f32 v[70:73], v107, v188, v[70:73]
	ds_read_b128 v[92:95], v90 offset:512
	ds_read_b128 v[96:99], v90 offset:576
	ds_read_b128 v[100:103], v90 offset:640
	ds_read_b128 v[104:107], v90 offset:704
	s_waitcnt lgkmcnt(3)
	s_waitcnt vmcnt(9)
	v_mfma_f32_16x16x4_f32 v[66:69], v92, v189, v[66:69]
	v_mfma_f32_16x16x4_f32 v[70:73], v92, v190, v[70:73]
	s_waitcnt vmcnt(7)
	v_mfma_f32_16x16x4_f32 v[66:69], v93, v191, v[66:69]
	v_mfma_f32_16x16x4_f32 v[70:73], v93, v192, v[70:73]
	s_waitcnt vmcnt(5)
	v_mfma_f32_16x16x4_f32 v[66:69], v94, v193, v[66:69]
	v_mfma_f32_16x16x4_f32 v[70:73], v94, v194, v[70:73]
	s_waitcnt vmcnt(3)
	v_mfma_f32_16x16x4_f32 v[66:69], v95, v195, v[66:69]
	v_mfma_f32_16x16x4_f32 v[70:73], v95, v196, v[70:73]
	s_waitcnt lgkmcnt(2)
	s_waitcnt vmcnt(1)
	v_mfma_f32_16x16x4_f32 v[66:69], v96, v197, v[66:69]
	v_mfma_f32_16x16x4_f32 v[70:73], v96, v198, v[70:73]
	s_waitcnt vmcnt(0)
	v_mfma_f32_16x16x4_f32 v[66:69], v97, v199, v[66:69]
	v_mfma_f32_16x16x4_f32 v[70:73], v97, v200, v[70:73]
	v_mfma_f32_16x16x4_f32 v[66:69], v98, v201, v[66:69]
	v_mfma_f32_16x16x4_f32 v[70:73], v98, v202, v[70:73]
	v_mfma_f32_16x16x4_f32 v[66:69], v99, v203, v[66:69]
	v_mfma_f32_16x16x4_f32 v[70:73], v99, v204, v[70:73]
	s_waitcnt lgkmcnt(1)
	v_mfma_f32_16x16x4_f32 v[66:69], v100, v205, v[66:69]
	v_mfma_f32_16x16x4_f32 v[70:73], v100, v206, v[70:73]
	v_mfma_f32_16x16x4_f32 v[66:69], v101, v207, v[66:69]
	v_mfma_f32_16x16x4_f32 v[70:73], v101, v208, v[70:73]
	v_mfma_f32_16x16x4_f32 v[66:69], v102, v209, v[66:69]
	v_mfma_f32_16x16x4_f32 v[70:73], v102, v210, v[70:73]
	v_mfma_f32_16x16x4_f32 v[66:69], v103, v211, v[66:69]
	v_mfma_f32_16x16x4_f32 v[70:73], v103, v212, v[70:73]
	s_waitcnt lgkmcnt(0)
	v_mfma_f32_16x16x4_f32 v[66:69], v104, v213, v[66:69]
	v_mfma_f32_16x16x4_f32 v[70:73], v104, v214, v[70:73]
	v_mfma_f32_16x16x4_f32 v[66:69], v105, v215, v[66:69]
	v_mfma_f32_16x16x4_f32 v[70:73], v105, v216, v[70:73]
	v_mfma_f32_16x16x4_f32 v[66:69], v106, v217, v[66:69]
	v_mfma_f32_16x16x4_f32 v[70:73], v106, v218, v[70:73]
	v_mfma_f32_16x16x4_f32 v[66:69], v107, v219, v[66:69]
	v_mfma_f32_16x16x4_f32 v[70:73], v107, v220, v[70:73]
	ds_read_b128 v[92:95], v90 offset:768
	ds_read_b128 v[96:99], v90 offset:832
	ds_read_b128 v[100:103], v90 offset:896
	ds_read_b128 v[104:107], v90 offset:960
	s_waitcnt lgkmcnt(3)
; #define LAS __attribute__((address_space(3)))
; template <bool SKIP_MIX>
; __device__ __forceinline__ void p8_ln_router(Frame& F0, const In& I) {
;     ...
;         for (int kk = 0; kk < 16; ++kk) {
;             const f32x4 a = *(const LAS f32x4*)(ap + 16 * kk);
; #pragma unroll
;             for (int e = 0; e < 4; ++e) {
;                 const float b0 = bp[(size_t)(16 * kk + e) * NE], b1 = bp[(size_t)(16 * kk + e) * NE + 16];
;                 c0 = __builtin_amdgcn_mfma_f32_16x16x4f32(a[e], b0, c0, 0, 0, 0);
;                 c1 = __builtin_amdgcn_mfma_f32_16x16x4f32(a[e], b1, c1, 0, 0, 0);
;             }
;         }
; #pragma unroll
;         for (int i = 0; i < 4; ++i) { part[(w * 16 + 4 * kq + i) * 32 + col] = c0[i]; part[(w * 16 + 4 * kq + i) * 32 + 16 + col] = c1[i]; }
;         __syncthreads();
;         { const int tl = F.tid >> 5, e = F.tid & 31; float s = I.b_router[e];
; #pragma unroll
;             for (int ww = 0; ww < 8; ++ww) s += part[(ww * 16 + tl) * 32 + e];
;             lg[tl * 32 + e] = s; }
;         __syncthreads();
;         if (F.tid < 16) {
;             const int tl = F.tid; float lv[32];
; #pragma unroll
;             for (int e = 0; e < 32; ++e) lv[e] = lg[tl * 32 + e];
;             int ti[4]; float tv[4];
; #pragma unroll
;             for (int k = 0; k < 4; ++k) { float best = -3.4e38f; int bi = 0;
; #pragma unroll
;                 for (int e = 0; e < 32; ++e) { const bool tk = lv[e] > best; best = tk ? lv[e] : best; bi = tk ? e : bi; }
	v_mfma_f32_16x16x4_f32 v[66:69], v92, v221, v[66:69]
	v_mfma_f32_16x16x4_f32 v[70:73], v92, v222, v[70:73]
	v_mfma_f32_16x16x4_f32 v[66:69], v93, v223, v[66:69]
	v_mfma_f32_16x16x4_f32 v[70:73], v93, v224, v[70:73]
	v_mfma_f32_16x16x4_f32 v[66:69], v94, v225, v[66:69]
	v_mfma_f32_16x16x4_f32 v[70:73], v94, v226, v[70:73]
	v_mfma_f32_16x16x4_f32 v[66:69], v95, v227, v[66:69]
	v_mfma_f32_16x16x4_f32 v[70:73], v95, v228, v[70:73]
	s_waitcnt lgkmcnt(2)
	v_mfma_f32_16x16x4_f32 v[66:69], v96, v229, v[66:69]
	v_mfma_f32_16x16x4_f32 v[70:73], v96, v230, v[70:73]
	v_mfma_f32_16x16x4_f32 v[66:69], v97, v231, v[66:69]
	v_mfma_f32_16x16x4_f32 v[70:73], v97, v232, v[70:73]
	v_mfma_f32_16x16x4_f32 v[66:69], v98, v233, v[66:69]
	v_mfma_f32_16x16x4_f32 v[70:73], v98, v234, v[70:73]
	v_mfma_f32_16x16x4_f32 v[66:69], v99, v235, v[66:69]
	v_mfma_f32_16x16x4_f32 v[70:73], v99, v236, v[70:73]
	s_waitcnt lgkmcnt(1)
	v_mfma_f32_16x16x4_f32 v[66:69], v100, v237, v[66:69]
	v_mfma_f32_16x16x4_f32 v[70:73], v100, v238, v[70:73]
	v_mfma_f32_16x16x4_f32 v[66:69], v101, v239, v[66:69]
	v_mfma_f32_16x16x4_f32 v[70:73], v101, v240, v[70:73]
	v_mfma_f32_16x16x4_f32 v[66:69], v102, v241, v[66:69]
	v_mfma_f32_16x16x4_f32 v[70:73], v102, v242, v[70:73]
	v_mfma_f32_16x16x4_f32 v[66:69], v103, v243, v[66:69]
	v_mfma_f32_16x16x4_f32 v[70:73], v103, v244, v[70:73]
	s_waitcnt lgkmcnt(0)
	v_mfma_f32_16x16x4_f32 v[66:69], v104, v245, v[66:69]
	v_mfma_f32_16x16x4_f32 v[70:73], v104, v246, v[70:73]
	v_mfma_f32_16x16x4_f32 v[66:69], v105, v247, v[66:69]
	v_mfma_f32_16x16x4_f32 v[70:73], v105, v248, v[70:73]
	v_mfma_f32_16x16x4_f32 v[66:69], v106, v249, v[66:69]
	v_mfma_f32_16x16x4_f32 v[70:73], v106, v250, v[70:73]
	v_mfma_f32_16x16x4_f32 v[66:69], v107, v251, v[66:69]
	v_mfma_f32_16x16x4_f32 v[70:73], v107, v252, v[70:73]
	s_nop 8
	ds_write2_b32 v156, v66, v70 offset1:16
	ds_write2_b32 v156, v67, v71 offset0:32 offset1:48
	ds_write2_b32 v156, v68, v72 offset0:64 offset1:80
	ds_write2_b32 v156, v69, v73 offset0:96 offset1:112
	s_waitcnt lgkmcnt(0)
	s_barrier
	ds_read2st64_b32 v[66:67], v153 offset1:8
	ds_read2st64_b32 v[68:69], v153 offset0:16 offset1:24
	ds_read2st64_b32 v[70:71], v153 offset0:32 offset1:40
	ds_read2st64_b32 v[72:73], v153 offset0:48 offset1:56
	s_waitcnt lgkmcnt(3)
	v_add_f32_e32 v66, v253, v66
	v_add_f32_e32 v66, v66, v67
	s_waitcnt lgkmcnt(2)
	v_add_f32_e32 v66, v66, v68
	v_add_f32_e32 v66, v66, v69
	s_waitcnt lgkmcnt(1)
	v_add_f32_e32 v66, v66, v70
	v_add_f32_e32 v66, v66, v71
	s_waitcnt lgkmcnt(0)
	v_add_f32_e32 v66, v66, v72
	v_add_f32_e32 v66, v66, v73
	ds_write_b32 v154, v66
	s_waitcnt lgkmcnt(0)
	s_barrier
	s_and_saveexec_b64 s[0:1], s[4:5]
	s_cbranch_execz .LBB0_1513
	s_setprio 3
	ds_read_b128 v[68:71], v157
	ds_read_b128 v[90:93], v157 offset:16
	ds_read_b128 v[94:97], v157 offset:32
	ds_read_b128 v[98:101], v157 offset:48
	ds_read_b128 v[102:105], v157 offset:64
	ds_read_b128 v[106:109], v157 offset:80
	ds_read_b128 v[110:113], v157 offset:96
	ds_read_b128 v[114:117], v157 offset:112
	s_waitcnt lgkmcnt(7)
	v_max_f32_e32 v66, v68, v68
	v_max_f32_e32 v66, 0xff7fc99e, v66
	v_cmp_gt_f32_e32 vcc, v69, v66
	s_nop 1
	v_cndmask_b32_e32 v66, v66, v69, vcc
	v_cndmask_b32_e64 v67, 0, 1, vcc
	v_cmp_gt_f32_e32 vcc, v70, v66
	s_nop 1
	v_cndmask_b32_e32 v66, v66, v70, vcc
	v_cndmask_b32_e64 v67, v67, 2, vcc
	v_cmp_gt_f32_e32 vcc, v71, v66
	s_nop 1
	v_cndmask_b32_e32 v66, v66, v71, vcc
	v_cndmask_b32_e64 v67, v67, 3, vcc
	s_waitcnt lgkmcnt(6)
	v_cmp_gt_f32_e32 vcc, v90, v66
	s_nop 1
	v_cndmask_b32_e32 v66, v66, v90, vcc
	v_cndmask_b32_e64 v67, v67, 4, vcc
	v_cmp_gt_f32_e32 vcc, v91, v66
	s_nop 1
	v_cndmask_b32_e32 v66, v66, v91, vcc
	v_cndmask_b32_e64 v67, v67, 5, vcc
	v_cmp_gt_f32_e32 vcc, v92, v66
	s_nop 1
	v_cndmask_b32_e32 v66, v66, v92, vcc
	v_cndmask_b32_e64 v67, v67, 6, vcc
	v_cmp_gt_f32_e32 vcc, v93, v66
	s_nop 1
	v_cndmask_b32_e32 v66, v66, v93, vcc
	v_cndmask_b32_e64 v67, v67, 7, vcc
	s_waitcnt lgkmcnt(5)
	v_cmp_gt_f32_e32 vcc, v94, v66
	s_nop 1
	v_cndmask_b32_e32 v66, v66, v94, vcc
	v_cndmask_b32_e64 v67, v67, 8, vcc
	v_cmp_gt_f32_e32 vcc, v95, v66
	s_nop 1
	v_cndmask_b32_e32 v66, v66, v95, vcc
	v_cndmask_b32_e64 v67, v67, 9, vcc
	v_cmp_gt_f32_e32 vcc, v96, v66
	s_nop 1
	v_cndmask_b32_e32 v66, v66, v96, vcc
	v_cndmask_b32_e64 v67, v67, 10, vcc
	v_cmp_gt_f32_e32 vcc, v97, v66
	s_nop 1
	v_cndmask_b32_e32 v66, v66, v97, vcc
	v_cndmask_b32_e64 v67, v67, 11, vcc
	s_waitcnt lgkmcnt(4)
	v_cmp_gt_f32_e32 vcc, v98, v66
	s_nop 1
	v_cndmask_b32_e32 v66, v66, v98, vcc
	v_cndmask_b32_e64 v67, v67, 12, vcc
	v_cmp_gt_f32_e32 vcc, v99, v66
	s_nop 1
	v_cndmask_b32_e32 v66, v66, v99, vcc
	v_cndmask_b32_e64 v67, v67, 13, vcc
	v_cmp_gt_f32_e32 vcc, v100, v66
	s_nop 1
	v_cndmask_b32_e32 v66, v66, v100, vcc
	v_cndmask_b32_e64 v67, v67, 14, vcc
	v_cmp_gt_f32_e32 vcc, v101, v66
	s_nop 1
	v_cndmask_b32_e32 v66, v66, v101, vcc
	v_cndmask_b32_e64 v67, v67, 15, vcc
	s_waitcnt lgkmcnt(3)
	v_cmp_gt_f32_e32 vcc, v102, v66
	s_nop 1
	v_cndmask_b32_e32 v66, v66, v102, vcc
	v_cndmask_b32_e64 v67, v67, 16, vcc
	v_cmp_gt_f32_e32 vcc, v103, v66
	s_nop 1
	v_cndmask_b32_e32 v66, v66, v103, vcc
	v_cndmask_b32_e64 v67, v67, 17, vcc
	v_cmp_gt_f32_e32 vcc, v104, v66
	s_nop 1
	v_cndmask_b32_e32 v66, v66, v104, vcc
	v_cndmask_b32_e64 v67, v67, 18, vcc
	v_cmp_gt_f32_e32 vcc, v105, v66
	s_nop 1
	v_cndmask_b32_e32 v66, v66, v105, vcc
	v_cndmask_b32_e64 v67, v67, 19, vcc
	s_waitcnt lgkmcnt(2)
; template <bool SKIP_MIX>
; __device__ __forceinline__ void p8_ln_router(Frame& F0, const In& I) {
;     ...
;             for (int k = 0; k < 4; ++k) { float best = -3.4e38f; int bi = 0;
; #pragma unroll
;                 for (int e = 0; e < 32; ++e) { const bool tk = lv[e] > best; best = tk ? lv[e] : best; bi = tk ? e : bi; }
;                 ti[k] = bi; tv[k] = best;
; #pragma unroll
;                 for (int e = 0; e < 32; ++e) lv[e] = (e == bi) ? -3.4e38f : lv[e]; }
	v_cmp_gt_f32_e32 vcc, v106, v66
	s_nop 1
	v_cndmask_b32_e32 v66, v66, v106, vcc
	v_cndmask_b32_e64 v67, v67, 20, vcc
	v_cmp_gt_f32_e32 vcc, v107, v66
	s_nop 1
	v_cndmask_b32_e32 v66, v66, v107, vcc
	v_cndmask_b32_e64 v67, v67, 21, vcc
	v_cmp_gt_f32_e32 vcc, v108, v66
	s_nop 1
	v_cndmask_b32_e32 v66, v66, v108, vcc
	v_cndmask_b32_e64 v67, v67, 22, vcc
	v_cmp_gt_f32_e32 vcc, v109, v66
	s_nop 1
	v_cndmask_b32_e32 v66, v66, v109, vcc
	v_cndmask_b32_e64 v67, v67, 23, vcc
	s_waitcnt lgkmcnt(1)
	v_cmp_gt_f32_e32 vcc, v110, v66
	s_nop 1
	v_cndmask_b32_e32 v66, v66, v110, vcc
	v_cndmask_b32_e64 v67, v67, 24, vcc
	v_cmp_gt_f32_e32 vcc, v111, v66
	s_nop 1
	v_cndmask_b32_e32 v66, v66, v111, vcc
	v_cndmask_b32_e64 v67, v67, 25, vcc
	v_cmp_gt_f32_e32 vcc, v112, v66
	s_nop 1
	v_cndmask_b32_e32 v66, v66, v112, vcc
	v_cndmask_b32_e64 v67, v67, 26, vcc
	v_cmp_gt_f32_e32 vcc, v113, v66
	s_nop 1
	v_cndmask_b32_e32 v66, v66, v113, vcc
	v_cndmask_b32_e64 v67, v67, 27, vcc
	s_waitcnt lgkmcnt(0)
	v_cmp_gt_f32_e32 vcc, v114, v66
	s_nop 1
	v_cndmask_b32_e32 v66, v66, v114, vcc
	v_cndmask_b32_e64 v67, v67, 28, vcc
	v_cmp_gt_f32_e32 vcc, v115, v66
	s_nop 1
	v_cndmask_b32_e32 v66, v66, v115, vcc
	v_cndmask_b32_e64 v67, v67, 29, vcc
	v_cmp_gt_f32_e32 vcc, v116, v66
	s_nop 1
	v_cndmask_b32_e32 v72, v66, v116, vcc
	v_cndmask_b32_e64 v67, v67, 30, vcc
	v_cmp_gt_f32_e32 vcc, v117, v72
	s_nop 1
	v_cndmask_b32_e64 v66, v67, 31, vcc
	v_cndmask_b32_e32 v73, v72, v117, vcc
	v_cmp_ne_u32_e32 vcc, 0, v66
	s_nop 1
	v_cndmask_b32_e32 v68, v159, v68, vcc
	v_cmp_ne_u32_e32 vcc, 1, v66
	v_max_f32_e32 v67, v68, v68
	v_max_f32_e32 v67, 0xff7fc99e, v67
	v_cndmask_b32_e32 v69, v159, v69, vcc
	v_cmp_ne_u32_e32 vcc, 2, v66
	s_nop 1
	v_cndmask_b32_e32 v70, v159, v70, vcc
	v_cmp_ne_u32_e32 vcc, 3, v66
	s_nop 1
	v_cndmask_b32_e32 v71, v159, v71, vcc
	v_cmp_ne_u32_e32 vcc, 4, v66
	s_nop 1
	v_cndmask_b32_e32 v72, v159, v90, vcc
	v_cmp_ne_u32_e32 vcc, 5, v66
	s_nop 1
	v_cndmask_b32_e32 v90, v159, v91, vcc
	v_cmp_ne_u32_e32 vcc, 6, v66
	s_nop 1
	v_cndmask_b32_e32 v91, v159, v92, vcc
	v_cmp_ne_u32_e32 vcc, 7, v66
	s_nop 1
	v_cndmask_b32_e32 v92, v159, v93, vcc
	v_cmp_ne_u32_e32 vcc, 8, v66
	s_nop 1
	v_cndmask_b32_e32 v93, v159, v94, vcc
	v_cmp_ne_u32_e32 vcc, 9, v66
	s_nop 1
	v_cndmask_b32_e32 v94, v159, v95, vcc
	v_cmp_ne_u32_e32 vcc, 10, v66
	s_nop 1
	v_cndmask_b32_e32 v95, v159, v96, vcc
	v_cmp_ne_u32_e32 vcc, 11, v66
	s_nop 1
	v_cndmask_b32_e32 v96, v159, v97, vcc
	v_cmp_ne_u32_e32 vcc, 12, v66
	s_nop 1
	v_cndmask_b32_e32 v97, v159, v98, vcc
	v_cmp_ne_u32_e32 vcc, 13, v66
	s_nop 1
	v_cndmask_b32_e32 v98, v159, v99, vcc
	v_cmp_ne_u32_e32 vcc, 14, v66
	s_nop 1
	v_cndmask_b32_e32 v99, v159, v100, vcc
	v_cmp_ne_u32_e32 vcc, 15, v66
	s_nop 1
	v_cndmask_b32_e32 v100, v159, v101, vcc
	v_cmp_ne_u32_e32 vcc, 16, v66
	s_nop 1
	v_cndmask_b32_e32 v101, v159, v102, vcc
	v_cmp_ne_u32_e32 vcc, 17, v66
	s_nop 1
	v_cndmask_b32_e32 v102, v159, v103, vcc
	v_cmp_ne_u32_e32 vcc, 18, v66
	s_nop 1
	v_cndmask_b32_e32 v103, v159, v104, vcc
	v_cmp_ne_u32_e32 vcc, 19, v66
	s_nop 1
	v_cndmask_b32_e32 v104, v159, v105, vcc
	v_cmp_ne_u32_e32 vcc, 20, v66
	s_nop 1
	v_cndmask_b32_e32 v105, v159, v106, vcc
	v_cmp_ne_u32_e32 vcc, 21, v66
	s_nop 1
	v_cndmask_b32_e32 v106, v159, v107, vcc
	v_cmp_ne_u32_e32 vcc, 22, v66
	s_nop 1
	v_cndmask_b32_e32 v107, v159, v108, vcc
	v_cmp_ne_u32_e32 vcc, 23, v66
	s_nop 1
	v_cndmask_b32_e32 v108, v159, v109, vcc
	v_cmp_ne_u32_e32 vcc, 24, v66
	s_nop 1
	v_cndmask_b32_e32 v109, v159, v110, vcc
	v_cmp_ne_u32_e32 vcc, 25, v66
	s_nop 1
	v_cndmask_b32_e32 v110, v159, v111, vcc
	v_cmp_ne_u32_e32 vcc, 26, v66
	s_nop 1
	v_cndmask_b32_e32 v111, v159, v112, vcc
	v_cmp_ne_u32_e32 vcc, 27, v66
	s_nop 1
	v_cndmask_b32_e32 v112, v159, v113, vcc
	v_cmp_ne_u32_e32 vcc, 28, v66
	s_nop 1
	v_cndmask_b32_e32 v113, v159, v114, vcc
	v_cmp_ne_u32_e32 vcc, 29, v66
	s_nop 1
	v_cndmask_b32_e32 v114, v159, v115, vcc
	v_cmp_ne_u32_e32 vcc, 30, v66
	s_nop 1
	v_cndmask_b32_e32 v115, v159, v116, vcc
	v_cmp_ne_u32_e32 vcc, 31, v66
	s_nop 1
	v_cndmask_b32_e32 v116, v159, v117, vcc
	v_cmp_gt_f32_e32 vcc, v69, v67
	s_nop 1
	v_cndmask_b32_e32 v67, v67, v69, vcc
	v_cndmask_b32_e64 v117, 0, 1, vcc
	v_cmp_gt_f32_e32 vcc, v70, v67
	s_nop 1
	v_cndmask_b32_e32 v67, v67, v70, vcc
	v_cndmask_b32_e64 v117, v117, 2, vcc
	v_cmp_gt_f32_e32 vcc, v71, v67
	s_nop 1
	v_cndmask_b32_e32 v67, v67, v71, vcc
	v_cndmask_b32_e64 v117, v117, 3, vcc
	v_cmp_gt_f32_e32 vcc, v72, v67
	s_nop 1
	v_cndmask_b32_e32 v67, v67, v72, vcc
	v_cndmask_b32_e64 v117, v117, 4, vcc
	v_cmp_gt_f32_e32 vcc, v90, v67
	s_nop 1
	v_cndmask_b32_e32 v67, v67, v90, vcc
	v_cndmask_b32_e64 v117, v117, 5, vcc
	v_cmp_gt_f32_e32 vcc, v91, v67
	s_nop 1
	v_cndmask_b32_e32 v67, v67, v91, vcc
	v_cndmask_b32_e64 v117, v117, 6, vcc
	v_cmp_gt_f32_e32 vcc, v92, v67
	s_nop 1
	v_cndmask_b32_e32 v67, v67, v92, vcc
	v_cndmask_b32_e64 v117, v117, 7, vcc
	v_cmp_gt_f32_e32 vcc, v93, v67
	s_nop 1
	v_cndmask_b32_e32 v67, v67, v93, vcc
	v_cndmask_b32_e64 v117, v117, 8, vcc
	v_cmp_gt_f32_e32 vcc, v94, v67
	s_nop 1
	v_cndmask_b32_e32 v67, v67, v94, vcc
	v_cndmask_b32_e64 v117, v117, 9, vcc
	v_cmp_gt_f32_e32 vcc, v95, v67
	s_nop 1
	v_cndmask_b32_e32 v67, v67, v95, vcc
	v_cndmask_b32_e64 v117, v117, 10, vcc
	v_cmp_gt_f32_e32 vcc, v96, v67
	s_nop 1
	v_cndmask_b32_e32 v67, v67, v96, vcc
	v_cndmask_b32_e64 v117, v117, 11, vcc
	v_cmp_gt_f32_e32 vcc, v97, v67
	s_nop 1
	v_cndmask_b32_e32 v67, v67, v97, vcc
	v_cndmask_b32_e64 v117, v117, 12, vcc
	v_cmp_gt_f32_e32 vcc, v98, v67
	s_nop 1
	v_cndmask_b32_e32 v67, v67, v98, vcc
	v_cndmask_b32_e64 v117, v117, 13, vcc
	v_cmp_gt_f32_e32 vcc, v99, v67
	s_nop 1
; template <bool SKIP_MIX>
; __device__ __forceinline__ void p8_ln_router(Frame& F0, const In& I) {
;     ...
;             for (int k = 0; k < 4; ++k) { float best = -3.4e38f; int bi = 0;
; #pragma unroll
;                 for (int e = 0; e < 32; ++e) { const bool tk = lv[e] > best; best = tk ? lv[e] : best; bi = tk ? e : bi; }
;                 ti[k] = bi; tv[k] = best;
; #pragma unroll
;                 for (int e = 0; e < 32; ++e) lv[e] = (e == bi) ? -3.4e38f : lv[e]; }
	v_cndmask_b32_e32 v67, v67, v99, vcc
	v_cndmask_b32_e64 v117, v117, 14, vcc
	v_cmp_gt_f32_e32 vcc, v100, v67
	s_nop 1
	v_cndmask_b32_e32 v67, v67, v100, vcc
	v_cndmask_b32_e64 v117, v117, 15, vcc
	v_cmp_gt_f32_e32 vcc, v101, v67
	s_nop 1
	v_cndmask_b32_e32 v67, v67, v101, vcc
	v_cndmask_b32_e64 v117, v117, 16, vcc
	v_cmp_gt_f32_e32 vcc, v102, v67
	s_nop 1
	v_cndmask_b32_e32 v67, v67, v102, vcc
	v_cndmask_b32_e64 v117, v117, 17, vcc
	v_cmp_gt_f32_e32 vcc, v103, v67
	s_nop 1
	v_cndmask_b32_e32 v67, v67, v103, vcc
	v_cndmask_b32_e64 v117, v117, 18, vcc
	v_cmp_gt_f32_e32 vcc, v104, v67
	s_nop 1
	v_cndmask_b32_e32 v67, v67, v104, vcc
	v_cndmask_b32_e64 v117, v117, 19, vcc
	v_cmp_gt_f32_e32 vcc, v105, v67
	s_nop 1
	v_cndmask_b32_e32 v67, v67, v105, vcc
	v_cndmask_b32_e64 v117, v117, 20, vcc
	v_cmp_gt_f32_e32 vcc, v106, v67
	s_nop 1
	v_cndmask_b32_e32 v67, v67, v106, vcc
	v_cndmask_b32_e64 v117, v117, 21, vcc
	v_cmp_gt_f32_e32 vcc, v107, v67
	s_nop 1
	v_cndmask_b32_e32 v67, v67, v107, vcc
	v_cndmask_b32_e64 v117, v117, 22, vcc
	v_cmp_gt_f32_e32 vcc, v108, v67
	s_nop 1
	v_cndmask_b32_e32 v67, v67, v108, vcc
	v_cndmask_b32_e64 v117, v117, 23, vcc
	v_cmp_gt_f32_e32 vcc, v109, v67
	s_nop 1
	v_cndmask_b32_e32 v67, v67, v109, vcc
	v_cndmask_b32_e64 v117, v117, 24, vcc
	v_cmp_gt_f32_e32 vcc, v110, v67
	s_nop 1
	v_cndmask_b32_e32 v67, v67, v110, vcc
	v_cndmask_b32_e64 v117, v117, 25, vcc
	v_cmp_gt_f32_e32 vcc, v111, v67
	s_nop 1
	v_cndmask_b32_e32 v67, v67, v111, vcc
	v_cndmask_b32_e64 v117, v117, 26, vcc
	v_cmp_gt_f32_e32 vcc, v112, v67
	s_nop 1
	v_cndmask_b32_e32 v67, v67, v112, vcc
	v_cndmask_b32_e64 v117, v117, 27, vcc
	v_cmp_gt_f32_e32 vcc, v113, v67
	s_nop 1
	v_cndmask_b32_e32 v67, v67, v113, vcc
	v_cndmask_b32_e64 v117, v117, 28, vcc
	v_cmp_gt_f32_e32 vcc, v114, v67
	s_nop 1
	v_cndmask_b32_e32 v67, v67, v114, vcc
	v_cndmask_b32_e64 v117, v117, 29, vcc
	v_cmp_gt_f32_e32 vcc, v115, v67
	s_nop 1
	v_cndmask_b32_e32 v118, v67, v115, vcc
	v_cndmask_b32_e64 v117, v117, 30, vcc
	v_cmp_gt_f32_e32 vcc, v116, v118
	s_nop 1
	v_cndmask_b32_e64 v67, v117, 31, vcc
	v_cndmask_b32_e32 v117, v118, v116, vcc
	v_cmp_ne_u32_e32 vcc, 0, v67
	s_nop 1
	v_cndmask_b32_e32 v118, v159, v68, vcc
	v_cmp_ne_u32_e32 vcc, 1, v67
	v_max_f32_e32 v68, v118, v118
	v_max_f32_e32 v68, 0xff7fc99e, v68
	v_cndmask_b32_e32 v69, v159, v69, vcc
	v_cmp_ne_u32_e32 vcc, 2, v67
	s_nop 1
	v_cndmask_b32_e32 v70, v159, v70, vcc
	v_cmp_ne_u32_e32 vcc, 3, v67
	s_nop 1
	v_cndmask_b32_e32 v71, v159, v71, vcc
	v_cmp_ne_u32_e32 vcc, 4, v67
	s_nop 1
	v_cndmask_b32_e32 v72, v159, v72, vcc
	v_cmp_ne_u32_e32 vcc, 5, v67
	s_nop 1
	v_cndmask_b32_e32 v90, v159, v90, vcc
	v_cmp_ne_u32_e32 vcc, 6, v67
	s_nop 1
	v_cndmask_b32_e32 v91, v159, v91, vcc
	v_cmp_ne_u32_e32 vcc, 7, v67
	s_nop 1
	v_cndmask_b32_e32 v92, v159, v92, vcc
	v_cmp_ne_u32_e32 vcc, 8, v67
	s_nop 1
	v_cndmask_b32_e32 v93, v159, v93, vcc
	v_cmp_ne_u32_e32 vcc, 9, v67
	s_nop 1
	v_cndmask_b32_e32 v94, v159, v94, vcc
	v_cmp_ne_u32_e32 vcc, 10, v67
	s_nop 1
	v_cndmask_b32_e32 v95, v159, v95, vcc
	v_cmp_ne_u32_e32 vcc, 11, v67
	s_nop 1
	v_cndmask_b32_e32 v96, v159, v96, vcc
	v_cmp_ne_u32_e32 vcc, 12, v67
	s_nop 1
	v_cndmask_b32_e32 v97, v159, v97, vcc
	v_cmp_ne_u32_e32 vcc, 13, v67
	s_nop 1
	v_cndmask_b32_e32 v98, v159, v98, vcc
	v_cmp_ne_u32_e32 vcc, 14, v67
	s_nop 1
	v_cndmask_b32_e32 v99, v159, v99, vcc
	v_cmp_ne_u32_e32 vcc, 15, v67
	s_nop 1
	v_cndmask_b32_e32 v100, v159, v100, vcc
	v_cmp_ne_u32_e32 vcc, 16, v67
	s_nop 1
	v_cndmask_b32_e32 v101, v159, v101, vcc
	v_cmp_ne_u32_e32 vcc, 17, v67
	s_nop 1
	v_cndmask_b32_e32 v102, v159, v102, vcc
	v_cmp_ne_u32_e32 vcc, 18, v67
	s_nop 1
	v_cndmask_b32_e32 v103, v159, v103, vcc
	v_cmp_ne_u32_e32 vcc, 19, v67
	s_nop 1
	v_cndmask_b32_e32 v104, v159, v104, vcc
	v_cmp_ne_u32_e32 vcc, 20, v67
	s_nop 1
	v_cndmask_b32_e32 v105, v159, v105, vcc
	v_cmp_ne_u32_e32 vcc, 21, v67
	s_nop 1
	v_cndmask_b32_e32 v106, v159, v106, vcc
	v_cmp_ne_u32_e32 vcc, 22, v67
	s_nop 1
	v_cndmask_b32_e32 v107, v159, v107, vcc
	v_cmp_ne_u32_e32 vcc, 23, v67
	s_nop 1
	v_cndmask_b32_e32 v108, v159, v108, vcc
	v_cmp_ne_u32_e32 vcc, 24, v67
	s_nop 1
	v_cndmask_b32_e32 v109, v159, v109, vcc
	v_cmp_ne_u32_e32 vcc, 25, v67
	s_nop 1
	v_cndmask_b32_e32 v110, v159, v110, vcc
	v_cmp_ne_u32_e32 vcc, 26, v67
	s_nop 1
	v_cndmask_b32_e32 v111, v159, v111, vcc
	v_cmp_ne_u32_e32 vcc, 27, v67
	s_nop 1
	v_cndmask_b32_e32 v112, v159, v112, vcc
	v_cmp_ne_u32_e32 vcc, 28, v67
	s_nop 1
	v_cndmask_b32_e32 v113, v159, v113, vcc
	v_cmp_ne_u32_e32 vcc, 29, v67
	s_nop 1
	v_cndmask_b32_e32 v114, v159, v114, vcc
	v_cmp_ne_u32_e32 vcc, 30, v67
	s_nop 1
	v_cndmask_b32_e32 v115, v159, v115, vcc
	v_cmp_ne_u32_e32 vcc, 31, v67
	s_nop 1
	v_cndmask_b32_e32 v116, v159, v116, vcc
	v_cmp_gt_f32_e32 vcc, v69, v68
	s_nop 1
	v_cndmask_b32_e32 v68, v68, v69, vcc
	v_cndmask_b32_e64 v119, 0, 1, vcc
	v_cmp_gt_f32_e32 vcc, v70, v68
	s_nop 1
	v_cndmask_b32_e32 v68, v68, v70, vcc
	v_cndmask_b32_e64 v119, v119, 2, vcc
	v_cmp_gt_f32_e32 vcc, v71, v68
	s_nop 1
	v_cndmask_b32_e32 v68, v68, v71, vcc
	v_cndmask_b32_e64 v119, v119, 3, vcc
	v_cmp_gt_f32_e32 vcc, v72, v68
	s_nop 1
	v_cndmask_b32_e32 v68, v68, v72, vcc
	v_cndmask_b32_e64 v119, v119, 4, vcc
	v_cmp_gt_f32_e32 vcc, v90, v68
	s_nop 1
	v_cndmask_b32_e32 v68, v68, v90, vcc
	v_cndmask_b32_e64 v119, v119, 5, vcc
	v_cmp_gt_f32_e32 vcc, v91, v68
	s_nop 1
	v_cndmask_b32_e32 v68, v68, v91, vcc
	v_cndmask_b32_e64 v119, v119, 6, vcc
	v_cmp_gt_f32_e32 vcc, v92, v68
	s_nop 1
	v_cndmask_b32_e32 v68, v68, v92, vcc
	v_cndmask_b32_e64 v119, v119, 7, vcc
	v_cmp_gt_f32_e32 vcc, v93, v68
	s_nop 1
	v_cndmask_b32_e32 v68, v68, v93, vcc
; template <bool SKIP_MIX>
; __device__ __forceinline__ void p8_ln_router(Frame& F0, const In& I) {
;     ...
;             for (int k = 0; k < 4; ++k) { float best = -3.4e38f; int bi = 0;
; #pragma unroll
;                 for (int e = 0; e < 32; ++e) { const bool tk = lv[e] > best; best = tk ? lv[e] : best; bi = tk ? e : bi; }
;                 ti[k] = bi; tv[k] = best;
; #pragma unroll
;                 for (int e = 0; e < 32; ++e) lv[e] = (e == bi) ? -3.4e38f : lv[e]; }
	v_cndmask_b32_e64 v119, v119, 8, vcc
	v_cmp_gt_f32_e32 vcc, v94, v68
	s_nop 1
	v_cndmask_b32_e32 v68, v68, v94, vcc
	v_cndmask_b32_e64 v119, v119, 9, vcc
	v_cmp_gt_f32_e32 vcc, v95, v68
	s_nop 1
	v_cndmask_b32_e32 v68, v68, v95, vcc
	v_cndmask_b32_e64 v119, v119, 10, vcc
	v_cmp_gt_f32_e32 vcc, v96, v68
	s_nop 1
	v_cndmask_b32_e32 v68, v68, v96, vcc
	v_cndmask_b32_e64 v119, v119, 11, vcc
	v_cmp_gt_f32_e32 vcc, v97, v68
	s_nop 1
	v_cndmask_b32_e32 v68, v68, v97, vcc
	v_cndmask_b32_e64 v119, v119, 12, vcc
	v_cmp_gt_f32_e32 vcc, v98, v68
	s_nop 1
	v_cndmask_b32_e32 v68, v68, v98, vcc
	v_cndmask_b32_e64 v119, v119, 13, vcc
	v_cmp_gt_f32_e32 vcc, v99, v68
	s_nop 1
	v_cndmask_b32_e32 v68, v68, v99, vcc
	v_cndmask_b32_e64 v119, v119, 14, vcc
	v_cmp_gt_f32_e32 vcc, v100, v68
	s_nop 1
	v_cndmask_b32_e32 v68, v68, v100, vcc
	v_cndmask_b32_e64 v119, v119, 15, vcc
	v_cmp_gt_f32_e32 vcc, v101, v68
	s_nop 1
	v_cndmask_b32_e32 v68, v68, v101, vcc
	v_cndmask_b32_e64 v119, v119, 16, vcc
	v_cmp_gt_f32_e32 vcc, v102, v68
	s_nop 1
	v_cndmask_b32_e32 v68, v68, v102, vcc
	v_cndmask_b32_e64 v119, v119, 17, vcc
	v_cmp_gt_f32_e32 vcc, v103, v68
	s_nop 1
	v_cndmask_b32_e32 v68, v68, v103, vcc
	v_cndmask_b32_e64 v119, v119, 18, vcc
	v_cmp_gt_f32_e32 vcc, v104, v68
	s_nop 1
	v_cndmask_b32_e32 v68, v68, v104, vcc
	v_cndmask_b32_e64 v119, v119, 19, vcc
	v_cmp_gt_f32_e32 vcc, v105, v68
	s_nop 1
	v_cndmask_b32_e32 v68, v68, v105, vcc
	v_cndmask_b32_e64 v119, v119, 20, vcc
	v_cmp_gt_f32_e32 vcc, v106, v68
	s_nop 1
	v_cndmask_b32_e32 v68, v68, v106, vcc
	v_cndmask_b32_e64 v119, v119, 21, vcc
	v_cmp_gt_f32_e32 vcc, v107, v68
	s_nop 1
	v_cndmask_b32_e32 v68, v68, v107, vcc
	v_cndmask_b32_e64 v119, v119, 22, vcc
	v_cmp_gt_f32_e32 vcc, v108, v68
	s_nop 1
	v_cndmask_b32_e32 v68, v68, v108, vcc
	v_cndmask_b32_e64 v119, v119, 23, vcc
	v_cmp_gt_f32_e32 vcc, v109, v68
	s_nop 1
	v_cndmask_b32_e32 v68, v68, v109, vcc
	v_cndmask_b32_e64 v119, v119, 24, vcc
	v_cmp_gt_f32_e32 vcc, v110, v68
	s_nop 1
	v_cndmask_b32_e32 v68, v68, v110, vcc
	v_cndmask_b32_e64 v119, v119, 25, vcc
	v_cmp_gt_f32_e32 vcc, v111, v68
	s_nop 1
	v_cndmask_b32_e32 v68, v68, v111, vcc
	v_cndmask_b32_e64 v119, v119, 26, vcc
	v_cmp_gt_f32_e32 vcc, v112, v68
	s_nop 1
	v_cndmask_b32_e32 v68, v68, v112, vcc
	v_cndmask_b32_e64 v119, v119, 27, vcc
	v_cmp_gt_f32_e32 vcc, v113, v68
	s_nop 1
	v_cndmask_b32_e32 v68, v68, v113, vcc
	v_cndmask_b32_e64 v119, v119, 28, vcc
	v_cmp_gt_f32_e32 vcc, v114, v68
	s_nop 1
	v_cndmask_b32_e32 v68, v68, v114, vcc
	v_cndmask_b32_e64 v119, v119, 29, vcc
	v_cmp_gt_f32_e32 vcc, v115, v68
	s_nop 1
	v_cndmask_b32_e32 v120, v68, v115, vcc
	v_cndmask_b32_e64 v119, v119, 30, vcc
	v_cmp_gt_f32_e32 vcc, v116, v120
	s_nop 1
	v_cndmask_b32_e64 v68, v119, 31, vcc
	v_cndmask_b32_e32 v119, v120, v116, vcc
	v_cmp_ne_u32_e32 vcc, 0, v68
	s_nop 1
	v_cndmask_b32_e32 v118, v159, v118, vcc
	v_cmp_ne_u32_e32 vcc, 1, v68
	v_max_f32_e32 v118, v118, v118
	v_max_f32_e32 v118, 0xff7fc99e, v118
	v_cndmask_b32_e32 v69, v159, v69, vcc
	v_cmp_ne_u32_e32 vcc, 2, v68
	s_nop 1
	v_cndmask_b32_e32 v70, v159, v70, vcc
	v_cmp_ne_u32_e32 vcc, 3, v68
	s_nop 1
	v_cndmask_b32_e32 v71, v159, v71, vcc
	v_cmp_ne_u32_e32 vcc, 4, v68
	s_nop 1
	v_cndmask_b32_e32 v72, v159, v72, vcc
	v_cmp_ne_u32_e32 vcc, 5, v68
	s_nop 1
	v_cndmask_b32_e32 v90, v159, v90, vcc
	v_cmp_ne_u32_e32 vcc, 6, v68
	s_nop 1
	v_cndmask_b32_e32 v91, v159, v91, vcc
	v_cmp_ne_u32_e32 vcc, 7, v68
	s_nop 1
	v_cndmask_b32_e32 v92, v159, v92, vcc
	v_cmp_ne_u32_e32 vcc, 8, v68
	s_nop 1
	v_cndmask_b32_e32 v93, v159, v93, vcc
	v_cmp_ne_u32_e32 vcc, 9, v68
	s_nop 1
	v_cndmask_b32_e32 v94, v159, v94, vcc
	v_cmp_ne_u32_e32 vcc, 10, v68
	s_nop 1
	v_cndmask_b32_e32 v95, v159, v95, vcc
	v_cmp_ne_u32_e32 vcc, 11, v68
	s_nop 1
	v_cndmask_b32_e32 v96, v159, v96, vcc
	v_cmp_ne_u32_e32 vcc, 12, v68
	s_nop 1
	v_cndmask_b32_e32 v97, v159, v97, vcc
	v_cmp_ne_u32_e32 vcc, 13, v68
	s_nop 1
	v_cndmask_b32_e32 v98, v159, v98, vcc
	v_cmp_ne_u32_e32 vcc, 14, v68
	s_nop 1
	v_cndmask_b32_e32 v99, v159, v99, vcc
	v_cmp_ne_u32_e32 vcc, 15, v68
	s_nop 1
	v_cndmask_b32_e32 v100, v159, v100, vcc
	v_cmp_ne_u32_e32 vcc, 16, v68
	s_nop 1
	v_cndmask_b32_e32 v101, v159, v101, vcc
	v_cmp_ne_u32_e32 vcc, 17, v68
	s_nop 1
	v_cndmask_b32_e32 v102, v159, v102, vcc
	v_cmp_ne_u32_e32 vcc, 18, v68
	s_nop 1
	v_cndmask_b32_e32 v103, v159, v103, vcc
	v_cmp_ne_u32_e32 vcc, 19, v68
	s_nop 1
	v_cndmask_b32_e32 v104, v159, v104, vcc
	v_cmp_ne_u32_e32 vcc, 20, v68
	s_nop 1
	v_cndmask_b32_e32 v105, v159, v105, vcc
	v_cmp_ne_u32_e32 vcc, 21, v68
	s_nop 1
	v_cndmask_b32_e32 v106, v159, v106, vcc
	v_cmp_ne_u32_e32 vcc, 22, v68
	s_nop 1
	v_cndmask_b32_e32 v107, v159, v107, vcc
	v_cmp_ne_u32_e32 vcc, 23, v68
	s_nop 1
	v_cndmask_b32_e32 v108, v159, v108, vcc
	v_cmp_ne_u32_e32 vcc, 24, v68
	s_nop 1
	v_cndmask_b32_e32 v109, v159, v109, vcc
	v_cmp_ne_u32_e32 vcc, 25, v68
	s_nop 1
	v_cndmask_b32_e32 v110, v159, v110, vcc
	v_cmp_ne_u32_e32 vcc, 26, v68
	s_nop 1
	v_cndmask_b32_e32 v111, v159, v111, vcc
	v_cmp_ne_u32_e32 vcc, 27, v68
	s_nop 1
	v_cndmask_b32_e32 v112, v159, v112, vcc
	v_cmp_ne_u32_e32 vcc, 28, v68
	s_nop 1
	v_cndmask_b32_e32 v113, v159, v113, vcc
	v_cmp_ne_u32_e32 vcc, 29, v68
	s_nop 1
	v_cndmask_b32_e32 v114, v159, v114, vcc
	v_cmp_ne_u32_e32 vcc, 30, v68
; #define GAS __attribute__((address_space(1)))
; template <bool SKIP_MIX>
; __device__ __forceinline__ void p8_ln_router(Frame& F0, const In& I) {
;     ...
;             for (int k = 0; k < 4; ++k) { float best = -3.4e38f; int bi = 0;
; #pragma unroll
;                 for (int e = 0; e < 32; ++e) { const bool tk = lv[e] > best; best = tk ? lv[e] : best; bi = tk ? e : bi; }
;                 ti[k] = bi; tv[k] = best;
; #pragma unroll
;                 for (int e = 0; e < 32; ++e) lv[e] = (e == bi) ? -3.4e38f : lv[e]; }
;             float ex[4], sum = 0.f;
; #pragma unroll
;             for (int k = 0; k < 4; ++k) { ex[k] = __expf(tv[k] - tv[0]); sum += ex[k]; }
;             const float inv = 1.f / sum;
;             *(GAS v4u*)((int*)(F.ws + WS_TOPI) + (size_t)(tok0 + tl) * 4) = (v4u){(unsigned)ti[0], (unsigned)ti[1], (unsigned)ti[2], (unsigned)ti[3]};
;             *(GAS f32x4*)((float*)(F.ws + WS_GATE) + (size_t)(tok0 + tl) * 4) = (f32x4){ex[0] * inv, ex[1] * inv, ex[2] * inv, ex[3] * inv};
; #pragma unroll
;             for (int k = 0; k < 4; ++k) __hip_atomic_fetch_add(&hist[ti[k]], 1, __ATOMIC_RELAXED, __HIP_MEMORY_SCOPE_WORKGROUP);
;         }
	s_nop 1
	v_cndmask_b32_e32 v115, v159, v115, vcc
	v_cmp_ne_u32_e32 vcc, 31, v68
	s_nop 1
	v_cndmask_b32_e32 v116, v159, v116, vcc
	v_cmp_gt_f32_e32 vcc, v69, v118
	s_nop 1
	v_cndmask_b32_e32 v69, v118, v69, vcc
	v_cndmask_b32_e64 v120, 0, 1, vcc
	v_cmp_gt_f32_e32 vcc, v70, v69
	s_nop 1
	v_cndmask_b32_e32 v69, v69, v70, vcc
	v_cndmask_b32_e64 v118, v120, 2, vcc
	v_cmp_gt_f32_e32 vcc, v71, v69
	s_nop 1
	v_cndmask_b32_e32 v69, v69, v71, vcc
	v_cndmask_b32_e64 v70, v118, 3, vcc
	v_cmp_gt_f32_e32 vcc, v72, v69
	s_nop 1
	v_cndmask_b32_e32 v69, v69, v72, vcc
	v_cndmask_b32_e64 v70, v70, 4, vcc
	v_cmp_gt_f32_e32 vcc, v90, v69
	v_sub_f32_e32 v72, v119, v73
	v_mul_f32_e32 v72, 0x3fb8aa3b, v72
	v_cndmask_b32_e32 v69, v69, v90, vcc
	v_cndmask_b32_e64 v70, v70, 5, vcc
	v_cmp_gt_f32_e32 vcc, v91, v69
	v_exp_f32_e32 v72, v72
	s_nop 0
	v_cndmask_b32_e32 v69, v69, v91, vcc
	v_cndmask_b32_e64 v70, v70, 6, vcc
	v_cmp_gt_f32_e32 vcc, v92, v69
	s_nop 1
	v_cndmask_b32_e32 v69, v69, v92, vcc
	v_cndmask_b32_e64 v70, v70, 7, vcc
	v_cmp_gt_f32_e32 vcc, v93, v69
	s_nop 1
	v_cndmask_b32_e32 v69, v69, v93, vcc
	v_cndmask_b32_e64 v70, v70, 8, vcc
	v_cmp_gt_f32_e32 vcc, v94, v69
	s_nop 1
	v_cndmask_b32_e32 v69, v69, v94, vcc
	v_cndmask_b32_e64 v70, v70, 9, vcc
	v_cmp_gt_f32_e32 vcc, v95, v69
	s_nop 1
	v_cndmask_b32_e32 v69, v69, v95, vcc
	v_cndmask_b32_e64 v70, v70, 10, vcc
	v_cmp_gt_f32_e32 vcc, v96, v69
	s_nop 1
	v_cndmask_b32_e32 v69, v69, v96, vcc
	v_cndmask_b32_e64 v70, v70, 11, vcc
	v_cmp_gt_f32_e32 vcc, v97, v69
	s_nop 1
	v_cndmask_b32_e32 v69, v69, v97, vcc
	v_cndmask_b32_e64 v70, v70, 12, vcc
	v_cmp_gt_f32_e32 vcc, v98, v69
	s_nop 1
	v_cndmask_b32_e32 v69, v69, v98, vcc
	v_cndmask_b32_e64 v70, v70, 13, vcc
	v_cmp_gt_f32_e32 vcc, v99, v69
	s_nop 1
	v_cndmask_b32_e32 v69, v69, v99, vcc
	v_cndmask_b32_e64 v70, v70, 14, vcc
	v_cmp_gt_f32_e32 vcc, v100, v69
	s_nop 1
	v_cndmask_b32_e32 v69, v69, v100, vcc
	v_cndmask_b32_e64 v70, v70, 15, vcc
	v_cmp_gt_f32_e32 vcc, v101, v69
	s_nop 1
	v_cndmask_b32_e32 v69, v69, v101, vcc
	v_cndmask_b32_e64 v70, v70, 16, vcc
	v_cmp_gt_f32_e32 vcc, v102, v69
	s_nop 1
	v_cndmask_b32_e32 v69, v69, v102, vcc
	v_cndmask_b32_e64 v70, v70, 17, vcc
	v_cmp_gt_f32_e32 vcc, v103, v69
	s_nop 1
	v_cndmask_b32_e32 v69, v69, v103, vcc
	v_cndmask_b32_e64 v70, v70, 18, vcc
	v_cmp_gt_f32_e32 vcc, v104, v69
	s_nop 1
	v_cndmask_b32_e32 v69, v69, v104, vcc
	v_cndmask_b32_e64 v70, v70, 19, vcc
	v_cmp_gt_f32_e32 vcc, v105, v69
	s_nop 1
	v_cndmask_b32_e32 v69, v69, v105, vcc
	v_cndmask_b32_e64 v70, v70, 20, vcc
	v_cmp_gt_f32_e32 vcc, v106, v69
	s_nop 1
	v_cndmask_b32_e32 v69, v69, v106, vcc
	v_cndmask_b32_e64 v70, v70, 21, vcc
	v_cmp_gt_f32_e32 vcc, v107, v69
	s_nop 1
	v_cndmask_b32_e32 v69, v69, v107, vcc
	v_cndmask_b32_e64 v70, v70, 22, vcc
	v_cmp_gt_f32_e32 vcc, v108, v69
	s_nop 1
	v_cndmask_b32_e32 v69, v69, v108, vcc
	v_cndmask_b32_e64 v70, v70, 23, vcc
	v_cmp_gt_f32_e32 vcc, v109, v69
	s_nop 1
	v_cndmask_b32_e32 v69, v69, v109, vcc
	v_cndmask_b32_e64 v70, v70, 24, vcc
	v_cmp_gt_f32_e32 vcc, v110, v69
	s_nop 1
	v_cndmask_b32_e32 v69, v69, v110, vcc
	v_cndmask_b32_e64 v70, v70, 25, vcc
	v_cmp_gt_f32_e32 vcc, v111, v69
	s_nop 1
	v_cndmask_b32_e32 v69, v69, v111, vcc
	v_cndmask_b32_e64 v70, v70, 26, vcc
	v_cmp_gt_f32_e32 vcc, v112, v69
	s_nop 1
	v_cndmask_b32_e32 v69, v69, v112, vcc
	v_cndmask_b32_e64 v70, v70, 27, vcc
	v_cmp_gt_f32_e32 vcc, v113, v69
	s_nop 1
	v_cndmask_b32_e32 v69, v69, v113, vcc
	v_cndmask_b32_e64 v70, v70, 28, vcc
	v_cmp_gt_f32_e32 vcc, v114, v69
	s_nop 1
	v_cndmask_b32_e32 v69, v69, v114, vcc
	v_cndmask_b32_e64 v70, v70, 29, vcc
	v_cmp_gt_f32_e32 vcc, v115, v69
	s_nop 1
	v_cndmask_b32_e32 v71, v69, v115, vcc
	v_cndmask_b32_e64 v70, v70, 30, vcc
	v_cmp_gt_f32_e32 vcc, v116, v71
	s_nop 1
	v_cndmask_b32_e64 v69, v70, 31, vcc
	v_sub_f32_e32 v70, v73, v73
	v_cndmask_b32_e32 v90, v71, v116, vcc
	v_mul_f32_e32 v70, 0x3fb8aa3b, v70
	v_sub_f32_e32 v71, v117, v73
	v_exp_f32_e32 v70, v70
	v_mul_f32_e32 v71, 0x3fb8aa3b, v71
	v_exp_f32_e32 v71, v71
	v_sub_f32_e32 v73, v90, v73
	v_mul_f32_e32 v73, 0x3fb8aa3b, v73
	v_exp_f32_e32 v73, v73
	v_add_f32_e32 v90, 0, v70
	v_add_f32_e32 v90, v90, v71
	v_add_f32_e32 v90, v90, v72
	v_add_f32_e32 v90, v90, v73
	v_div_scale_f32 v91, s[14:15], v90, v90, 1.0
	v_rcp_f32_e32 v92, v91
	s_nop 0
	v_fma_f32 v93, -v91, v92, 1.0
	v_fmac_f32_e32 v92, v93, v92
	v_div_scale_f32 v93, vcc, 1.0, v90, 1.0
	v_mul_f32_e32 v94, v93, v92
	v_fma_f32 v95, -v91, v94, v93
	v_fmac_f32_e32 v94, v95, v92
	v_fma_f32 v91, -v91, v94, v93
	v_div_fmas_f32 v91, v91, v92, v94
	v_add_u32_e32 v92, s23, v74
	v_ashrrev_i32_e32 v93, 31, v92
	v_div_fixup_f32 v90, v91, v90, 1.0
	v_lshlrev_b64 v[92:93], 4, v[92:93]
	v_lshl_add_u64 v[94:95], s[6:7], 0, v[92:93]
	v_pk_mul_f32 v[72:73], v[72:73], v[90:91] op_sel_hi:[1,0]
	v_pk_mul_f32 v[70:71], v[70:71], v[90:91] op_sel_hi:[1,0]
	v_lshl_add_u64 v[90:91], s[10:11], 0, v[92:93]
	global_store_dwordx4 v[94:95], v[66:69], off
	global_store_dwordx4 v[90:91], v[70:73], off
	s_nop 0
	v_lshl_add_u32 v66, v66, 2, s21
	ds_add_u32 v66, v158
	v_lshl_add_u32 v66, v67, 2, s21
	ds_add_u32 v66, v158
	v_lshl_add_u32 v66, v68, 2, s21
	ds_add_u32 v66, v158
	v_lshl_add_u32 v66, v69, 2, s21
	ds_add_u32 v66, v158
	s_setprio 0
	s_branch .LBB0_1513
